# P9 slice fetches take the SGPR base directly (26 v_lshl_add_u64 per item removed), on top of v99
# baseline (speedup 1.0000x reference)
.LBB0_1503:
	s_or_b64 exec, exec, s[48:49]
	s_ashr_i32 s45, s44, 31
	v_readlane_b32 s43, v254, 9
	s_ashr_i32 s47, s46, 31
	s_add_i32 s53, s53, s43
	s_lshl_b64 s[44:45], s[44:45], 7
	s_lshl_b64 s[46:47], s[46:47], 17
	s_add_u32 s46, s31, s46
	s_addc_u32 s47, s33, s47
	ds_write_b128 v173, v[22:25]
	s_waitcnt lgkmcnt(0)
	ds_write_b128 v174, v[2:5]
	ds_write_b128 v175, v[6:9]
	ds_write_b128 v176, v[10:13]
	ds_write_b128 v177, v[14:17] offset:128
	ds_write_b128 v178, v[18:21] offset:128
	ds_write_b128 v179, v[26:29] offset:128
	ds_write_b128 v180, v[30:33] offset:128
	ds_write_b128 v181, v[34:37] offset:256
	ds_write_b128 v182, v[38:41] offset:256
	ds_write_b128 v183, v[42:45] offset:256
	ds_write_b128 v184, v[46:49] offset:256
	ds_write_b128 v185, v[50:53] offset:384
	ds_write_b128 v186, v[54:57] offset:384
	ds_write_b128 v187, v[58:61] offset:384
	ds_write_b128 v188, v[62:65] offset:384
	global_load_dwordx4 v[22:25], v66, s[46:47] nt
	global_load_dwordx4 v[2:5], v66, s[46:47] offset:1024 nt
	global_load_dwordx4 v[6:9], v66, s[46:47] offset:2048 nt
	s_nop 0
	global_load_dwordx4 v[10:13], v66, s[46:47] offset:3072 nt
	s_nop 0
	global_load_dwordx4 v[14:17], v74, s[46:47] nt
	s_nop 0
	global_load_dwordx4 v[18:21], v76, s[46:47] nt
	s_nop 0
	global_load_dwordx4 v[26:29], v78, s[46:47] nt
	s_nop 0
	global_load_dwordx4 v[30:33], v80, s[46:47] nt
	s_nop 0
	global_load_dwordx4 v[34:37], v82, s[46:47] nt
	s_nop 0
	global_load_dwordx4 v[38:41], v84, s[46:47] nt
	s_nop 0
	global_load_dwordx4 v[42:45], v86, s[46:47] nt
	s_nop 0
	global_load_dwordx4 v[46:49], v88, s[46:47] nt
	ds_read2_b64 v[60:63], v189 offset1:16
	s_waitcnt lgkmcnt(14)
	v_pk_fma_f32 v[148:149], v[148:149], 0, v[152:153] op_sel_hi:[1,0,1]
	v_pk_fma_f32 v[144:145], v[148:149], v[144:145], v[150:151]
	s_waitcnt lgkmcnt(0)
	v_lshlrev_b32_e32 v64, 16, v60
	v_pk_fma_f32 v[140:141], v[144:145], v[140:141], v[146:147]
	v_lshlrev_b32_e32 v65, 16, v61
	v_add_f32_e32 v144, 0, v64
	v_pk_fma_f32 v[138:139], v[140:141], v[138:139], v[142:143]
	v_exp_f32_e32 v142, v64
	v_add_f32_e32 v145, 0, v65
	v_exp_f32_e32 v143, v65
	v_lshlrev_b32_e32 v64, 16, v62
	v_lshlrev_b32_e32 v65, 16, v63
	global_load_dwordx4 v[50:53], v90, s[46:47] nt
	s_nop 0
	global_load_dwordx4 v[54:57], v92, s[46:47] nt
	v_add_f32_e32 v148, v144, v64
	v_add_f32_e32 v149, v145, v65
	ds_read2_b64 v[144:147], v189 offset0:32 offset1:48
	v_exp_f32_e32 v64, v64
	v_exp_f32_e32 v65, v65
	v_and_b32_e32 v141, 0xffff0000, v60
	v_fma_f32 v60, 0, v142, v141
	v_and_b32_e32 v140, 0xffff0000, v61
	v_and_b32_e32 v62, 0xffff0000, v62
	v_fma_f32 v61, 0, v143, v140
	v_fmac_f32_e32 v62, v64, v60
	v_and_b32_e32 v60, 0xffff0000, v63
	s_waitcnt lgkmcnt(0)
	v_lshlrev_b32_e32 v63, 16, v145
	v_fmac_f32_e32 v60, v65, v61
	v_lshlrev_b32_e32 v61, 16, v144
	v_add_f32_e32 v65, v149, v63
	v_add_f32_e32 v64, v148, v61
	v_exp_f32_e32 v63, v63
	v_exp_f32_e32 v61, v61
	v_and_b32_e32 v145, 0xffff0000, v145
	v_and_b32_e32 v144, 0xffff0000, v144
	v_fmac_f32_e32 v145, v63, v60
	v_lshlrev_b32_e32 v60, 16, v146
	v_fmac_f32_e32 v144, v61, v62
	v_lshlrev_b32_e32 v61, 16, v147
	v_add_f32_e32 v64, v64, v60
	v_exp_f32_e32 v148, v60
	v_add_f32_e32 v65, v65, v61
	v_exp_f32_e32 v149, v61
	ds_read2_b64 v[60:63], v189 offset0:64 offset1:80
	v_and_b32_e32 v146, 0xffff0000, v146
	v_fmac_f32_e32 v146, v148, v144
	v_and_b32_e32 v144, 0xffff0000, v147
	v_fmac_f32_e32 v144, v149, v145
	s_waitcnt lgkmcnt(0)
	v_lshlrev_b32_e32 v147, 16, v61
	v_lshlrev_b32_e32 v145, 16, v60
	v_add_f32_e32 v65, v65, v147
	v_add_f32_e32 v64, v64, v145
	v_exp_f32_e32 v147, v147
	v_exp_f32_e32 v145, v145
	v_and_b32_e32 v61, 0xffff0000, v61
	v_and_b32_e32 v60, 0xffff0000, v60
	v_fmac_f32_e32 v61, v147, v144
	v_lshlrev_b32_e32 v144, 16, v62
	v_fmac_f32_e32 v60, v145, v146
	v_lshlrev_b32_e32 v145, 16, v63
	v_add_f32_e32 v64, v64, v144
	v_exp_f32_e32 v148, v144
	v_add_f32_e32 v65, v65, v145
	v_exp_f32_e32 v149, v145
	ds_read2_b64 v[144:147], v189 offset0:96 offset1:112
	v_and_b32_e32 v62, 0xffff0000, v62
	v_fmac_f32_e32 v62, v148, v60
	v_and_b32_e32 v60, 0xffff0000, v63
	v_fmac_f32_e32 v60, v149, v61
	s_waitcnt lgkmcnt(0)
	v_lshlrev_b32_e32 v63, 16, v145
	v_lshlrev_b32_e32 v61, 16, v144
	v_add_f32_e32 v65, v65, v63
	v_add_f32_e32 v64, v64, v61
	v_exp_f32_e32 v63, v63
	v_exp_f32_e32 v61, v61
	v_and_b32_e32 v145, 0xffff0000, v145
	v_and_b32_e32 v144, 0xffff0000, v144
	v_fmac_f32_e32 v145, v63, v60
	v_lshlrev_b32_e32 v60, 16, v146
	v_fmac_f32_e32 v144, v61, v62
	v_lshlrev_b32_e32 v61, 16, v147
	v_add_f32_e32 v64, v64, v60
	v_exp_f32_e32 v148, v60
	v_add_f32_e32 v65, v65, v61
	v_exp_f32_e32 v149, v61
	ds_read2_b64 v[60:63], v189 offset0:128 offset1:144
	v_and_b32_e32 v146, 0xffff0000, v146
	v_fmac_f32_e32 v146, v148, v144
	v_and_b32_e32 v144, 0xffff0000, v147
	v_fmac_f32_e32 v144, v149, v145
	s_waitcnt lgkmcnt(0)
	v_lshlrev_b32_e32 v147, 16, v61
	v_lshlrev_b32_e32 v145, 16, v60
	v_add_f32_e32 v65, v65, v147
	v_add_f32_e32 v64, v64, v145
	v_exp_f32_e32 v147, v147
	v_exp_f32_e32 v145, v145
	v_and_b32_e32 v61, 0xffff0000, v61
	v_and_b32_e32 v60, 0xffff0000, v60
	v_fmac_f32_e32 v61, v147, v144
	v_lshlrev_b32_e32 v144, 16, v62
	v_fmac_f32_e32 v60, v145, v146
	v_lshlrev_b32_e32 v145, 16, v63
	v_add_f32_e32 v64, v64, v144
	v_exp_f32_e32 v148, v144
	v_add_f32_e32 v65, v65, v145
	v_exp_f32_e32 v149, v145
	ds_read2_b64 v[144:147], v189 offset0:160 offset1:176
	v_and_b32_e32 v62, 0xffff0000, v62
	v_fmac_f32_e32 v62, v148, v60
	v_and_b32_e32 v60, 0xffff0000, v63
	v_fmac_f32_e32 v60, v149, v61
	s_waitcnt lgkmcnt(0)
	v_lshlrev_b32_e32 v63, 16, v145
	v_lshlrev_b32_e32 v61, 16, v144
	v_add_f32_e32 v65, v65, v63
	v_add_f32_e32 v64, v64, v61
	v_exp_f32_e32 v63, v63
	v_exp_f32_e32 v61, v61
	v_and_b32_e32 v145, 0xffff0000, v145
	v_and_b32_e32 v144, 0xffff0000, v144
	v_fmac_f32_e32 v145, v63, v60
	v_lshlrev_b32_e32 v60, 16, v146
	v_fmac_f32_e32 v144, v61, v62
	v_lshlrev_b32_e32 v61, 16, v147
	v_add_f32_e32 v64, v64, v60
	v_exp_f32_e32 v148, v60
	v_add_f32_e32 v65, v65, v61
	v_exp_f32_e32 v149, v61
	ds_read2_b64 v[60:63], v189 offset0:192 offset1:208
	v_and_b32_e32 v146, 0xffff0000, v146
	v_fmac_f32_e32 v146, v148, v144
	v_and_b32_e32 v144, 0xffff0000, v147
	v_fmac_f32_e32 v144, v149, v145
	s_waitcnt lgkmcnt(0)
	v_lshlrev_b32_e32 v147, 16, v61
	v_lshlrev_b32_e32 v145, 16, v60
	v_add_f32_e32 v65, v65, v147
	v_add_f32_e32 v64, v64, v145
	v_exp_f32_e32 v147, v147
	v_exp_f32_e32 v145, v145
	v_and_b32_e32 v61, 0xffff0000, v61
	v_and_b32_e32 v60, 0xffff0000, v60
	v_fmac_f32_e32 v61, v147, v144
	v_lshlrev_b32_e32 v144, 16, v62
	v_fmac_f32_e32 v60, v145, v146
	v_lshlrev_b32_e32 v145, 16, v63
	v_add_f32_e32 v64, v64, v144
	v_exp_f32_e32 v148, v144
	v_add_f32_e32 v65, v65, v145
	v_exp_f32_e32 v149, v145
	ds_read2_b64 v[144:147], v189 offset0:224 offset1:240
	v_and_b32_e32 v62, 0xffff0000, v62
	v_fmac_f32_e32 v62, v148, v60
	v_and_b32_e32 v60, 0xffff0000, v63
	v_fmac_f32_e32 v60, v149, v61
	s_waitcnt lgkmcnt(0)
	v_lshlrev_b32_e32 v63, 16, v145
	v_lshlrev_b32_e32 v61, 16, v144
	v_add_f32_e32 v65, v65, v63
	v_add_f32_e32 v64, v64, v61
	v_exp_f32_e32 v63, v63
	v_exp_f32_e32 v61, v61
	v_and_b32_e32 v145, 0xffff0000, v145
	v_and_b32_e32 v144, 0xffff0000, v144
	v_fmac_f32_e32 v145, v63, v60
	v_lshlrev_b32_e32 v60, 16, v146
	v_fmac_f32_e32 v144, v61, v62
	v_lshlrev_b32_e32 v61, 16, v147
	v_add_f32_e32 v64, v64, v60
	v_exp_f32_e32 v148, v60
	v_add_u32_e32 v150, 0x800, v189
	v_add_f32_e32 v65, v65, v61
	v_exp_f32_e32 v149, v61
	ds_read2_b64 v[60:63], v150 offset1:16
	v_and_b32_e32 v146, 0xffff0000, v146
	v_fmac_f32_e32 v146, v148, v144
	v_and_b32_e32 v144, 0xffff0000, v147
	v_fmac_f32_e32 v144, v149, v145
	s_waitcnt lgkmcnt(0)
	v_lshlrev_b32_e32 v147, 16, v61
	v_lshlrev_b32_e32 v145, 16, v60
	v_add_f32_e32 v65, v65, v147
	v_add_f32_e32 v64, v64, v145
	v_exp_f32_e32 v147, v147
	v_exp_f32_e32 v145, v145
	v_and_b32_e32 v61, 0xffff0000, v61
	v_and_b32_e32 v60, 0xffff0000, v60
	v_fmac_f32_e32 v61, v147, v144
	v_lshlrev_b32_e32 v144, 16, v62
	v_fmac_f32_e32 v60, v145, v146
	v_lshlrev_b32_e32 v145, 16, v63
	v_add_f32_e32 v64, v64, v144
	v_exp_f32_e32 v148, v144
	v_add_f32_e32 v65, v65, v145
	v_exp_f32_e32 v149, v145
	ds_read2_b64 v[144:147], v150 offset0:32 offset1:48
	v_and_b32_e32 v62, 0xffff0000, v62
	v_fmac_f32_e32 v62, v148, v60
	v_and_b32_e32 v60, 0xffff0000, v63
	v_fmac_f32_e32 v60, v149, v61
	s_waitcnt lgkmcnt(0)
	v_lshlrev_b32_e32 v63, 16, v145
	v_lshlrev_b32_e32 v61, 16, v144
	v_add_f32_e32 v65, v65, v63
	v_add_f32_e32 v64, v64, v61
	v_exp_f32_e32 v63, v63
	v_exp_f32_e32 v61, v61
	v_and_b32_e32 v145, 0xffff0000, v145
	v_and_b32_e32 v144, 0xffff0000, v144
	v_fmac_f32_e32 v145, v63, v60
	v_lshlrev_b32_e32 v60, 16, v146
	v_fmac_f32_e32 v144, v61, v62
	v_lshlrev_b32_e32 v61, 16, v147
	v_add_f32_e32 v64, v64, v60
	v_exp_f32_e32 v148, v60
	v_add_f32_e32 v65, v65, v61
	v_exp_f32_e32 v149, v61
	ds_read2_b64 v[60:63], v150 offset0:64 offset1:80
	v_and_b32_e32 v146, 0xffff0000, v146
	v_fmac_f32_e32 v146, v148, v144
	v_and_b32_e32 v144, 0xffff0000, v147
	v_fmac_f32_e32 v144, v149, v145
	s_waitcnt lgkmcnt(0)
	v_lshlrev_b32_e32 v147, 16, v61
	v_lshlrev_b32_e32 v145, 16, v60
	v_add_f32_e32 v65, v65, v147
	v_add_f32_e32 v64, v64, v145
	v_exp_f32_e32 v147, v147
	v_exp_f32_e32 v145, v145
	v_and_b32_e32 v61, 0xffff0000, v61
	v_and_b32_e32 v60, 0xffff0000, v60
	v_fmac_f32_e32 v61, v147, v144
	v_lshlrev_b32_e32 v144, 16, v62
	v_fmac_f32_e32 v60, v145, v146
	v_lshlrev_b32_e32 v145, 16, v63
	v_add_f32_e32 v64, v64, v144
	v_exp_f32_e32 v148, v144
	v_add_f32_e32 v65, v65, v145
	v_exp_f32_e32 v149, v145
	ds_read2_b64 v[144:147], v150 offset0:96 offset1:112
	v_and_b32_e32 v62, 0xffff0000, v62
	v_fmac_f32_e32 v62, v148, v60
	v_and_b32_e32 v60, 0xffff0000, v63
	v_fmac_f32_e32 v60, v149, v61
	s_waitcnt lgkmcnt(0)
	v_lshlrev_b32_e32 v63, 16, v145
	v_lshlrev_b32_e32 v61, 16, v144
	v_add_f32_e32 v65, v65, v63
	v_add_f32_e32 v64, v64, v61
	v_exp_f32_e32 v63, v63
	v_exp_f32_e32 v61, v61
	v_and_b32_e32 v145, 0xffff0000, v145
	v_and_b32_e32 v144, 0xffff0000, v144
	v_fmac_f32_e32 v145, v63, v60
	v_lshlrev_b32_e32 v60, 16, v146
	v_fmac_f32_e32 v144, v61, v62
	v_lshlrev_b32_e32 v61, 16, v147
	v_add_f32_e32 v64, v64, v60
	v_exp_f32_e32 v148, v60
	v_add_f32_e32 v65, v65, v61
	v_exp_f32_e32 v149, v61
	ds_read2_b64 v[60:63], v150 offset0:128 offset1:144
	v_and_b32_e32 v146, 0xffff0000, v146
	v_fmac_f32_e32 v146, v148, v144
	v_and_b32_e32 v144, 0xffff0000, v147
	v_fmac_f32_e32 v144, v149, v145
	s_waitcnt lgkmcnt(0)
	v_lshlrev_b32_e32 v147, 16, v61
	v_lshlrev_b32_e32 v145, 16, v60
	v_add_f32_e32 v65, v65, v147
	v_add_f32_e32 v64, v64, v145
	v_exp_f32_e32 v147, v147
	v_exp_f32_e32 v145, v145
	v_and_b32_e32 v61, 0xffff0000, v61
	v_and_b32_e32 v60, 0xffff0000, v60
	v_fmac_f32_e32 v61, v147, v144
	v_lshlrev_b32_e32 v144, 16, v62
	v_fmac_f32_e32 v60, v145, v146
	v_lshlrev_b32_e32 v145, 16, v63
	v_add_f32_e32 v64, v64, v144
	v_exp_f32_e32 v148, v144
	v_add_f32_e32 v65, v65, v145
	v_exp_f32_e32 v149, v145
	ds_read2_b64 v[144:147], v150 offset0:160 offset1:176
	v_and_b32_e32 v62, 0xffff0000, v62
	v_fmac_f32_e32 v62, v148, v60
	v_and_b32_e32 v60, 0xffff0000, v63
	v_fmac_f32_e32 v60, v149, v61
	s_waitcnt lgkmcnt(0)
	v_lshlrev_b32_e32 v63, 16, v145
	v_lshlrev_b32_e32 v61, 16, v144
	v_add_f32_e32 v65, v65, v63
	v_add_f32_e32 v64, v64, v61
	v_exp_f32_e32 v63, v63
	v_exp_f32_e32 v61, v61
	v_and_b32_e32 v145, 0xffff0000, v145
	v_and_b32_e32 v144, 0xffff0000, v144
	v_fmac_f32_e32 v145, v63, v60
	v_lshlrev_b32_e32 v60, 16, v146
	v_fmac_f32_e32 v144, v61, v62
	v_lshlrev_b32_e32 v61, 16, v147
	v_add_f32_e32 v64, v64, v60
	v_exp_f32_e32 v148, v60
	v_add_f32_e32 v65, v65, v61
	v_exp_f32_e32 v149, v61
	ds_read2_b64 v[60:63], v150 offset0:192 offset1:208
	v_and_b32_e32 v146, 0xffff0000, v146
	v_fmac_f32_e32 v146, v148, v144
	v_and_b32_e32 v144, 0xffff0000, v147
	v_fmac_f32_e32 v144, v149, v145
	s_waitcnt lgkmcnt(0)
	v_lshlrev_b32_e32 v147, 16, v61
	v_lshlrev_b32_e32 v145, 16, v60
	v_add_f32_e32 v65, v65, v147
	v_add_f32_e32 v64, v64, v145
	v_exp_f32_e32 v147, v147
	v_exp_f32_e32 v145, v145
	v_and_b32_e32 v61, 0xffff0000, v61
	v_and_b32_e32 v60, 0xffff0000, v60
	v_fmac_f32_e32 v61, v147, v144
	v_lshlrev_b32_e32 v144, 16, v62
	v_fmac_f32_e32 v60, v145, v146
	v_lshlrev_b32_e32 v145, 16, v63
	v_add_f32_e32 v64, v64, v144
	v_exp_f32_e32 v148, v144
	v_add_f32_e32 v65, v65, v145
	v_exp_f32_e32 v149, v145
	ds_read2_b64 v[144:147], v150 offset0:224 offset1:240
	v_and_b32_e32 v62, 0xffff0000, v62
	v_fmac_f32_e32 v62, v148, v60
	v_and_b32_e32 v60, 0xffff0000, v63
	v_fmac_f32_e32 v60, v149, v61
	s_waitcnt lgkmcnt(0)
	v_lshlrev_b32_e32 v61, 16, v144
	v_lshlrev_b32_e32 v63, 16, v145
	v_add_f32_e32 v64, v64, v61
	v_add_f32_e32 v65, v65, v63
	v_exp_f32_e32 v61, v61
	v_exp_f32_e32 v63, v63
	v_and_b32_e32 v144, 0xffff0000, v144
	v_fmac_f32_e32 v144, v61, v62
	v_and_b32_e32 v61, 0xffff0000, v145
	v_fmac_f32_e32 v61, v63, v60
	v_lshlrev_b32_e32 v60, 16, v146
	v_exp_f32_e32 v63, v60
	v_lshlrev_b32_e32 v62, 16, v147
	v_add_f32_e32 v60, v64, v60
	v_add_f32_e32 v64, v65, v62
	v_and_b32_e32 v145, 0xffff0000, v146
	v_fmac_f32_e32 v145, v63, v144
	v_exp_f32_e32 v62, v62
	v_exp_f32_e32 v144, v60
	v_exp_f32_e32 v146, v64
	v_and_b32_e32 v147, 0xffff0000, v147
	v_fmac_f32_e32 v147, v62, v61
	ds_bpermute_b32 v148, v73, v144
	ds_bpermute_b32 v149, v73, v146
	ds_bpermute_b32 v150, v73, v145
	ds_bpermute_b32 v151, v73, v147
	global_load_dwordx4 v[58:61], v94, s[46:47] nt
	s_nop 0
	global_load_dwordx4 v[62:65], v96, s[46:47] nt
	s_waitcnt lgkmcnt(1)
	v_fmac_f32_e32 v150, v138, v148
	s_waitcnt lgkmcnt(0)
	v_fmac_f32_e32 v151, v139, v149
	ds_bpermute_b32 v148, v166, v144
	ds_bpermute_b32 v149, v166, v145
	v_cndmask_b32_e64 v139, v151, v139, s[0:1]
	v_cndmask_b32_e64 v138, v150, v138, s[0:1]
	ds_bpermute_b32 v150, v166, v146
	ds_bpermute_b32 v151, v166, v147
	ds_bpermute_b32 v144, v167, v144
	ds_bpermute_b32 v146, v167, v146
	ds_bpermute_b32 v145, v167, v145
	ds_bpermute_b32 v147, v167, v147
	s_waitcnt lgkmcnt(6)
	v_fmac_f32_e32 v149, v138, v148
	s_waitcnt lgkmcnt(4)
	v_fmac_f32_e32 v151, v139, v150
	v_cndmask_b32_e64 v139, v139, v151, s[4:5]
	v_cndmask_b32_e64 v138, v138, v149, s[4:5]
	s_waitcnt lgkmcnt(1)
	v_fmac_f32_e32 v145, v138, v144
	s_waitcnt lgkmcnt(0)
	v_fmac_f32_e32 v147, v139, v146
	v_cndmask_b32_e64 v139, v139, v147, s[6:7]
	v_cndmask_b32_e64 v138, v138, v145, s[6:7]
	v_fmac_f32_e32 v141, v142, v138
	v_fmac_f32_e32 v140, v143, v139
	v_cvt_pk_bf16_f32 v138, v141, v140
	ds_read_b64 v[142:143], v189 offset:128
	s_cmpk_gt_i32 s53, 0x27ff
	s_waitcnt lgkmcnt(0)
	v_lshlrev_b32_e32 v139, 16, v142
	v_lshlrev_b32_e32 v144, 16, v143
	v_exp_f32_e32 v139, v139
	v_exp_f32_e32 v144, v144
	v_and_b32_e32 v142, 0xffff0000, v142
	v_and_b32_e32 v143, 0xffff0000, v143
	v_fmac_f32_e32 v142, v141, v139
	v_fmac_f32_e32 v143, v140, v144
	v_cvt_pk_bf16_f32 v139, v142, v143
	ds_read_b64 v[140:141], v189 offset:256
	s_waitcnt lgkmcnt(0)
	v_lshlrev_b32_e32 v144, 16, v140
	v_lshlrev_b32_e32 v145, 16, v141
	v_exp_f32_e32 v144, v144
	v_exp_f32_e32 v145, v145
	v_and_b32_e32 v146, 0xffff0000, v140
	v_and_b32_e32 v141, 0xffff0000, v141
	v_fmac_f32_e32 v146, v142, v144
	v_fmac_f32_e32 v141, v143, v145
	v_cvt_pk_bf16_f32 v140, v146, v141
	ds_read_b64 v[142:143], v189 offset:384
	s_waitcnt lgkmcnt(0)
	v_lshlrev_b32_e32 v144, 16, v142
	v_lshlrev_b32_e32 v145, 16, v143
	v_exp_f32_e32 v144, v144
	v_exp_f32_e32 v145, v145
	v_and_b32_e32 v147, 0xffff0000, v142
	v_fmac_f32_e32 v147, v146, v144
	v_and_b32_e32 v144, 0xffff0000, v143
	v_fmac_f32_e32 v144, v141, v145
	v_cvt_pk_bf16_f32 v141, v147, v144
	ds_read_b64 v[142:143], v189 offset:512
	s_waitcnt lgkmcnt(0)
	v_lshlrev_b32_e32 v145, 16, v142
	v_lshlrev_b32_e32 v146, 16, v143
	v_exp_f32_e32 v145, v145
	v_exp_f32_e32 v146, v146
	v_and_b32_e32 v148, 0xffff0000, v142
	v_and_b32_e32 v143, 0xffff0000, v143
	v_fmac_f32_e32 v148, v147, v145
	v_fmac_f32_e32 v143, v144, v146
	v_cvt_pk_bf16_f32 v142, v148, v143
	ds_read_b64 v[144:145], v189 offset:640
	s_waitcnt lgkmcnt(0)
	v_lshlrev_b32_e32 v146, 16, v144
	v_lshlrev_b32_e32 v147, 16, v145
	v_exp_f32_e32 v146, v146
	v_exp_f32_e32 v147, v147
	v_and_b32_e32 v149, 0xffff0000, v144
	v_fmac_f32_e32 v149, v148, v146
	v_and_b32_e32 v146, 0xffff0000, v145
	v_fmac_f32_e32 v146, v143, v147
	v_cvt_pk_bf16_f32 v143, v149, v146
	ds_read_b64 v[144:145], v189 offset:768
	s_waitcnt lgkmcnt(0)
	v_lshlrev_b32_e32 v147, 16, v144
	v_lshlrev_b32_e32 v148, 16, v145
	v_exp_f32_e32 v147, v147
	v_exp_f32_e32 v148, v148
	v_and_b32_e32 v150, 0xffff0000, v144
	v_and_b32_e32 v145, 0xffff0000, v145
	v_fmac_f32_e32 v150, v149, v147
	v_fmac_f32_e32 v145, v146, v148
	v_cvt_pk_bf16_f32 v144, v150, v145
	ds_read_b64 v[146:147], v189 offset:896
	s_waitcnt lgkmcnt(0)
	v_lshlrev_b32_e32 v148, 16, v146
	v_lshlrev_b32_e32 v149, 16, v147
	v_exp_f32_e32 v148, v148
	v_exp_f32_e32 v149, v149
	v_and_b32_e32 v151, 0xffff0000, v146
	v_and_b32_e32 v147, 0xffff0000, v147
	v_fmac_f32_e32 v151, v150, v148
	v_fmac_f32_e32 v147, v145, v149
	v_cvt_pk_bf16_f32 v146, v151, v147
	ds_read_b64 v[148:149], v189 offset:1024
	s_waitcnt lgkmcnt(0)
	v_lshlrev_b32_e32 v145, 16, v148
	v_lshlrev_b32_e32 v150, 16, v149
	v_exp_f32_e32 v145, v145
	v_exp_f32_e32 v150, v150
	v_and_b32_e32 v152, 0xffff0000, v148
	v_fmac_f32_e32 v152, v151, v145
	v_and_b32_e32 v145, 0xffff0000, v149
	v_fmac_f32_e32 v145, v147, v150
	v_cvt_pk_bf16_f32 v148, v152, v145
	ds_read_b64 v[150:151], v189 offset:1152
	s_waitcnt lgkmcnt(0)
	v_lshlrev_b32_e32 v147, 16, v150
	v_lshlrev_b32_e32 v149, 16, v151
	v_exp_f32_e32 v147, v147
	v_exp_f32_e32 v149, v149
	v_and_b32_e32 v154, 0xffff0000, v150
	v_fmac_f32_e32 v154, v152, v147
	v_and_b32_e32 v147, 0xffff0000, v151
	v_fmac_f32_e32 v147, v145, v149
	v_cvt_pk_bf16_f32 v150, v154, v147
	ds_read_b64 v[152:153], v189 offset:1280
	s_waitcnt lgkmcnt(0)
	v_lshlrev_b32_e32 v145, 16, v152
	v_lshlrev_b32_e32 v149, 16, v153
	v_exp_f32_e32 v145, v145
	v_exp_f32_e32 v149, v149
	v_and_b32_e32 v151, 0xffff0000, v152
	v_fmac_f32_e32 v151, v154, v145
	v_and_b32_e32 v145, 0xffff0000, v153
	v_fmac_f32_e32 v145, v147, v149
	v_cvt_pk_bf16_f32 v152, v151, v145
	ds_read_b64 v[154:155], v189 offset:1408
	s_waitcnt lgkmcnt(0)
	v_lshlrev_b32_e32 v147, 16, v154
	v_lshlrev_b32_e32 v149, 16, v155
	v_exp_f32_e32 v147, v147
	v_exp_f32_e32 v149, v149
	v_and_b32_e32 v153, 0xffff0000, v154
	v_fmac_f32_e32 v153, v151, v147
	v_and_b32_e32 v147, 0xffff0000, v155
	v_fmac_f32_e32 v147, v145, v149
	v_cvt_pk_bf16_f32 v155, v153, v147
	ds_read_b64 v[156:157], v189 offset:1536
	s_waitcnt lgkmcnt(0)
	v_lshlrev_b32_e32 v145, 16, v156
	v_lshlrev_b32_e32 v149, 16, v157
	v_exp_f32_e32 v145, v145
	v_exp_f32_e32 v149, v149
	v_and_b32_e32 v151, 0xffff0000, v156
	v_fmac_f32_e32 v151, v153, v145
	v_and_b32_e32 v145, 0xffff0000, v157
	v_fmac_f32_e32 v145, v147, v149
	v_cvt_pk_bf16_f32 v157, v151, v145
	ds_read_b64 v[194:195], v189 offset:1664
	s_waitcnt lgkmcnt(0)
	v_lshlrev_b32_e32 v147, 16, v194
	v_lshlrev_b32_e32 v149, 16, v195
	v_exp_f32_e32 v147, v147
	v_exp_f32_e32 v149, v149
	v_and_b32_e32 v153, 0xffff0000, v194
	v_fmac_f32_e32 v153, v151, v147
	v_and_b32_e32 v147, 0xffff0000, v195
	v_fmac_f32_e32 v147, v145, v149
	v_cvt_pk_bf16_f32 v194, v153, v147
	ds_read_b64 v[196:197], v189 offset:1792
	s_waitcnt lgkmcnt(0)
	v_lshlrev_b32_e32 v145, 16, v196
	v_lshlrev_b32_e32 v149, 16, v197
	v_exp_f32_e32 v145, v145
	v_exp_f32_e32 v149, v149
	v_and_b32_e32 v151, 0xffff0000, v196
	v_fmac_f32_e32 v151, v153, v145
	v_and_b32_e32 v145, 0xffff0000, v197
	v_fmac_f32_e32 v145, v147, v149
	v_cvt_pk_bf16_f32 v196, v151, v145
	ds_read_b64 v[198:199], v189 offset:1920
	s_waitcnt lgkmcnt(0)
	v_lshlrev_b32_e32 v147, 16, v198
	v_lshlrev_b32_e32 v149, 16, v199
	v_exp_f32_e32 v147, v147
	v_exp_f32_e32 v149, v149
	v_and_b32_e32 v153, 0xffff0000, v198
	v_fmac_f32_e32 v153, v151, v147
	v_and_b32_e32 v147, 0xffff0000, v199
	v_fmac_f32_e32 v147, v145, v149
	v_cvt_pk_bf16_f32 v198, v153, v147
	ds_read_b64 v[200:201], v189 offset:2048
	s_waitcnt lgkmcnt(0)
	v_lshlrev_b32_e32 v145, 16, v200
	v_lshlrev_b32_e32 v149, 16, v201
	v_exp_f32_e32 v145, v145
	v_exp_f32_e32 v149, v149
	v_and_b32_e32 v151, 0xffff0000, v200
	v_fmac_f32_e32 v151, v153, v145
	v_and_b32_e32 v145, 0xffff0000, v201
	v_fmac_f32_e32 v145, v147, v149
	v_cvt_pk_bf16_f32 v201, v151, v145
	ds_read_b64 v[202:203], v189 offset:2176
	s_waitcnt lgkmcnt(0)
	v_lshlrev_b32_e32 v147, 16, v202
	v_lshlrev_b32_e32 v149, 16, v203
	v_exp_f32_e32 v147, v147
	v_exp_f32_e32 v149, v149
	v_and_b32_e32 v153, 0xffff0000, v202
	v_fmac_f32_e32 v153, v151, v147
	v_and_b32_e32 v147, 0xffff0000, v203
	v_fmac_f32_e32 v147, v145, v149
	v_cvt_pk_bf16_f32 v203, v153, v147
	ds_read_b64 v[204:205], v189 offset:2304
	s_waitcnt lgkmcnt(0)
	v_lshlrev_b32_e32 v145, 16, v204
	v_lshlrev_b32_e32 v149, 16, v205
	v_exp_f32_e32 v145, v145
	v_exp_f32_e32 v149, v149
	v_and_b32_e32 v151, 0xffff0000, v204
	v_fmac_f32_e32 v151, v153, v145
	v_and_b32_e32 v145, 0xffff0000, v205
	v_fmac_f32_e32 v145, v147, v149
	v_cvt_pk_bf16_f32 v205, v151, v145
	ds_read_b64 v[206:207], v189 offset:2432
	s_waitcnt lgkmcnt(0)
	v_lshlrev_b32_e32 v147, 16, v206
	v_lshlrev_b32_e32 v149, 16, v207
	v_exp_f32_e32 v147, v147
	v_exp_f32_e32 v149, v149
	v_and_b32_e32 v153, 0xffff0000, v206
	v_fmac_f32_e32 v153, v151, v147
	v_and_b32_e32 v147, 0xffff0000, v207
	v_fmac_f32_e32 v147, v145, v149
	v_cvt_pk_bf16_f32 v207, v153, v147
	ds_read_b64 v[208:209], v189 offset:2560
	s_waitcnt lgkmcnt(0)
	v_lshlrev_b32_e32 v145, 16, v208
	v_lshlrev_b32_e32 v149, 16, v209
	v_exp_f32_e32 v145, v145
	v_exp_f32_e32 v149, v149
	v_and_b32_e32 v151, 0xffff0000, v208
	v_fmac_f32_e32 v151, v153, v145
	v_and_b32_e32 v145, 0xffff0000, v209
	v_fmac_f32_e32 v145, v147, v149
	v_cvt_pk_bf16_f32 v209, v151, v145
	ds_read_b64 v[210:211], v189 offset:2688
	s_waitcnt lgkmcnt(0)
	v_lshlrev_b32_e32 v147, 16, v210
	v_lshlrev_b32_e32 v149, 16, v211
	v_exp_f32_e32 v147, v147
	v_exp_f32_e32 v149, v149
	v_and_b32_e32 v153, 0xffff0000, v210
	v_fmac_f32_e32 v153, v151, v147
	v_and_b32_e32 v147, 0xffff0000, v211
	v_fmac_f32_e32 v147, v145, v149
	v_cvt_pk_bf16_f32 v211, v153, v147
	ds_read_b64 v[212:213], v189 offset:2816
	s_waitcnt lgkmcnt(0)
	v_lshlrev_b32_e32 v145, 16, v212
	v_lshlrev_b32_e32 v149, 16, v213
	v_exp_f32_e32 v145, v145
	v_exp_f32_e32 v149, v149
	v_and_b32_e32 v151, 0xffff0000, v212
	v_fmac_f32_e32 v151, v153, v145
	v_and_b32_e32 v145, 0xffff0000, v213
	v_fmac_f32_e32 v145, v147, v149
	v_cvt_pk_bf16_f32 v214, v151, v145
	ds_read_b64 v[212:213], v189 offset:2944
	s_waitcnt lgkmcnt(0)
	v_lshlrev_b32_e32 v147, 16, v212
	v_lshlrev_b32_e32 v149, 16, v213
	v_exp_f32_e32 v147, v147
	v_exp_f32_e32 v149, v149
	v_and_b32_e32 v153, 0xffff0000, v212
	v_fmac_f32_e32 v153, v151, v147
	v_and_b32_e32 v147, 0xffff0000, v213
	v_fmac_f32_e32 v147, v145, v149
	v_cvt_pk_bf16_f32 v216, v153, v147
	ds_read_b64 v[212:213], v189 offset:3072
	s_waitcnt lgkmcnt(0)
	v_lshlrev_b32_e32 v145, 16, v212
	v_lshlrev_b32_e32 v149, 16, v213
	v_exp_f32_e32 v145, v145
	v_exp_f32_e32 v149, v149
	v_and_b32_e32 v151, 0xffff0000, v212
	v_fmac_f32_e32 v151, v153, v145
	v_and_b32_e32 v145, 0xffff0000, v213
	v_fmac_f32_e32 v145, v147, v149
	v_cvt_pk_bf16_f32 v218, v151, v145
	ds_read_b64 v[212:213], v189 offset:3200
	s_waitcnt lgkmcnt(0)
	v_lshlrev_b32_e32 v147, 16, v212
	v_lshlrev_b32_e32 v149, 16, v213
	v_exp_f32_e32 v147, v147
	v_exp_f32_e32 v149, v149
	v_and_b32_e32 v153, 0xffff0000, v212
	v_fmac_f32_e32 v153, v151, v147
	v_and_b32_e32 v147, 0xffff0000, v213
	v_fmac_f32_e32 v147, v145, v149
	v_cvt_pk_bf16_f32 v220, v153, v147
	ds_read_b64 v[212:213], v189 offset:3328
	s_waitcnt lgkmcnt(0)
	v_lshlrev_b32_e32 v145, 16, v212
	v_lshlrev_b32_e32 v149, 16, v213
	v_exp_f32_e32 v145, v145
	v_exp_f32_e32 v149, v149
	v_and_b32_e32 v151, 0xffff0000, v212
	v_fmac_f32_e32 v151, v153, v145
	v_and_b32_e32 v145, 0xffff0000, v213
	v_fmac_f32_e32 v145, v147, v149
	v_cvt_pk_bf16_f32 v222, v151, v145
	ds_read_b64 v[212:213], v189 offset:3456
	s_waitcnt lgkmcnt(0)
	v_lshlrev_b32_e32 v147, 16, v212
	v_lshlrev_b32_e32 v149, 16, v213
	v_exp_f32_e32 v147, v147
	v_exp_f32_e32 v149, v149
	v_and_b32_e32 v153, 0xffff0000, v212
	v_fmac_f32_e32 v153, v151, v147
	v_and_b32_e32 v147, 0xffff0000, v213
	v_fmac_f32_e32 v147, v145, v149
	v_cvt_pk_bf16_f32 v225, v153, v147
	ds_read_b64 v[212:213], v189 offset:3584
	s_waitcnt lgkmcnt(0)
	v_lshlrev_b32_e32 v145, 16, v212
	v_lshlrev_b32_e32 v149, 16, v213
	v_exp_f32_e32 v145, v145
	v_exp_f32_e32 v149, v149
	v_and_b32_e32 v151, 0xffff0000, v212
	v_fmac_f32_e32 v151, v153, v145
	v_and_b32_e32 v145, 0xffff0000, v213
	v_fmac_f32_e32 v145, v147, v149
	v_cvt_pk_bf16_f32 v227, v151, v145
	ds_read_b64 v[212:213], v189 offset:3712
	s_waitcnt lgkmcnt(0)
	v_lshlrev_b32_e32 v147, 16, v212
	v_lshlrev_b32_e32 v149, 16, v213
	v_exp_f32_e32 v147, v147
	v_exp_f32_e32 v149, v149
	v_and_b32_e32 v153, 0xffff0000, v212
	v_fmac_f32_e32 v153, v151, v147
	v_and_b32_e32 v147, 0xffff0000, v213
	v_fmac_f32_e32 v147, v145, v149
	v_cvt_pk_bf16_f32 v229, v153, v147
	ds_read_b64 v[212:213], v189 offset:3840
	s_waitcnt lgkmcnt(0)
	v_lshlrev_b32_e32 v145, 16, v212
	v_lshlrev_b32_e32 v149, 16, v213
	v_exp_f32_e32 v145, v145
	v_exp_f32_e32 v149, v149
	v_and_b32_e32 v151, 0xffff0000, v212
	v_fmac_f32_e32 v151, v153, v145
	v_and_b32_e32 v145, 0xffff0000, v213
	v_fmac_f32_e32 v145, v147, v149
	v_cvt_pk_bf16_f32 v231, v151, v145
	ds_read_b64 v[212:213], v189 offset:3968
	s_waitcnt lgkmcnt(0)
	v_lshlrev_b32_e32 v147, 16, v212
	v_lshlrev_b32_e32 v149, 16, v213
	v_exp_f32_e32 v147, v147
	v_exp_f32_e32 v149, v149
	v_and_b32_e32 v153, 0xffff0000, v212
	v_fmac_f32_e32 v153, v151, v147
	v_and_b32_e32 v147, 0xffff0000, v213
	v_fmac_f32_e32 v147, v145, v149
	v_or_b32_e32 v145, s44, v68
	v_mov_b64_e32 v[212:213], s[12:13]
	v_mad_u64_u32 v[212:213], s[46:47], v145, s3, v[212:213]
	v_mad_i32_i24 v213, s45, v169, v213
	v_lshl_add_u64 v[100:101], v[100:101], 1, v[212:213]
	v_cvt_pk_bf16_f32 v233, v153, v147
	global_load_dword v145, v[100:101], off
	v_lshl_add_u64 v[100:101], v[100:101], 0, s[38:39]
	global_load_dword v147, v[100:101], off
	v_lshl_add_u64 v[100:101], v[100:101], 0, s[38:39]
	global_load_dword v149, v[100:101], off
	v_lshl_add_u64 v[100:101], v[100:101], 0, s[38:39]
	global_load_dword v151, v[100:101], off
	v_lshl_add_u64 v[100:101], v[100:101], 0, s[38:39]
	global_load_dword v153, v[100:101], off
	v_lshl_add_u64 v[100:101], v[100:101], 0, s[38:39]
	global_load_dword v154, v[100:101], off
	v_lshl_add_u64 v[100:101], v[100:101], 0, s[38:39]
	global_load_dword v156, v[100:101], off
	v_lshl_add_u64 v[100:101], v[100:101], 0, s[38:39]
	global_load_dword v193, v[100:101], off
	v_lshl_add_u64 v[100:101], v[100:101], 0, s[38:39]
	global_load_dword v195, v[100:101], off
	v_lshl_add_u64 v[100:101], v[100:101], 0, s[38:39]
	global_load_dword v197, v[100:101], off
	v_lshl_add_u64 v[100:101], v[100:101], 0, s[38:39]
	global_load_dword v199, v[100:101], off
	v_lshl_add_u64 v[100:101], v[100:101], 0, s[38:39]
	global_load_dword v200, v[100:101], off
	v_lshl_add_u64 v[100:101], v[100:101], 0, s[38:39]
	global_load_dword v202, v[100:101], off
	v_lshl_add_u64 v[100:101], v[100:101], 0, s[38:39]
	global_load_dword v204, v[100:101], off
	v_lshl_add_u64 v[100:101], v[100:101], 0, s[38:39]
	global_load_dword v206, v[100:101], off
	v_lshl_add_u64 v[100:101], v[100:101], 0, s[38:39]
	global_load_dword v208, v[100:101], off
	v_lshl_add_u64 v[100:101], v[100:101], 0, s[38:39]
	global_load_dword v210, v[100:101], off
	v_lshl_add_u64 v[100:101], v[100:101], 0, s[38:39]
	global_load_dword v212, v[100:101], off
	v_lshl_add_u64 v[100:101], v[100:101], 0, s[38:39]
	global_load_dword v213, v[100:101], off
	v_lshl_add_u64 v[100:101], v[100:101], 0, s[38:39]
	global_load_dword v215, v[100:101], off
	v_lshl_add_u64 v[100:101], v[100:101], 0, s[38:39]
	global_load_dword v217, v[100:101], off
	v_lshl_add_u64 v[100:101], v[100:101], 0, s[38:39]
	global_load_dword v219, v[100:101], off
	v_lshl_add_u64 v[100:101], v[100:101], 0, s[38:39]
	global_load_dword v221, v[100:101], off
	v_lshl_add_u64 v[100:101], v[100:101], 0, s[38:39]
	global_load_dword v223, v[100:101], off
	v_lshl_add_u64 v[100:101], v[100:101], 0, s[38:39]
	global_load_dword v224, v[100:101], off
	v_lshl_add_u64 v[100:101], v[100:101], 0, s[38:39]
	global_load_dword v226, v[100:101], off
	v_lshl_add_u64 v[100:101], v[100:101], 0, s[38:39]
	global_load_dword v228, v[100:101], off
	v_lshl_add_u64 v[100:101], v[100:101], 0, s[38:39]
	global_load_dword v230, v[100:101], off
	v_lshl_add_u64 v[100:101], v[100:101], 0, s[38:39]
	global_load_dword v232, v[100:101], off
	v_lshl_add_u64 v[100:101], v[100:101], 0, s[38:39]
	global_load_dword v234, v[100:101], off
	v_lshl_add_u64 v[100:101], v[100:101], 0, s[38:39]
	global_load_dword v235, v[100:101], off
	v_lshl_add_u64 v[100:101], v[100:101], 0, s[38:39]
	global_load_dword v236, v[100:101], off
	s_waitcnt vmcnt(32)
	v_pk_fma_f32 v[100:101], v[102:103], 0, v[106:107] op_sel_hi:[1,0,1]
	v_pk_mul_f32 v[102:103], v[102:103], v[110:111]
	v_pk_fma_f32 v[100:101], v[100:101], v[110:111], v[104:105]
	v_pk_mul_f32 v[102:103], v[102:103], v[108:109]
	v_pk_fma_f32 v[100:101], v[100:101], v[108:109], v[114:115]
	v_pk_mul_f32 v[102:103], v[102:103], v[118:119]
	v_pk_fma_f32 v[100:101], v[100:101], v[118:119], v[112:113]
	v_pk_mul_f32 v[102:103], v[102:103], v[116:117]
	v_pk_fma_f32 v[100:101], v[100:101], v[116:117], v[122:123]
	v_pk_mul_f32 v[102:103], v[102:103], v[126:127]
	v_pk_fma_f32 v[100:101], v[100:101], v[126:127], v[120:121]
	v_pk_mul_f32 v[102:103], v[102:103], v[124:125]
	v_pk_fma_f32 v[100:101], v[100:101], v[124:125], v[130:131]
	v_pk_mul_f32 v[102:103], v[102:103], v[134:135]
	v_pk_fma_f32 v[100:101], v[100:101], v[134:135], v[128:129]
	v_pk_mul_f32 v[108:109], v[102:103], v[132:133]
	v_pk_fma_f32 v[110:111], v[100:101], v[132:133], v[136:137]
	ds_bpermute_b32 v112, v73, v108
	ds_bpermute_b32 v113, v73, v109
	ds_bpermute_b32 v114, v73, v110
	ds_bpermute_b32 v115, v73, v111
	ds_bpermute_b32 v100, v166, v108
	ds_bpermute_b32 v101, v166, v109
	ds_bpermute_b32 v102, v166, v110
	ds_bpermute_b32 v103, v166, v111
	ds_bpermute_b32 v104, v167, v108
	ds_bpermute_b32 v105, v167, v109
	ds_bpermute_b32 v106, v167, v110
	ds_bpermute_b32 v107, v167, v111
	ds_bpermute_b32 v108, v168, v108
	ds_bpermute_b32 v109, v168, v109
	ds_bpermute_b32 v110, v168, v110
	ds_bpermute_b32 v111, v168, v111
	s_cselect_b64 s[46:47], -1, 0
	s_and_b64 vcc, exec, s[46:47]
	ds_write_b128 v173, v[22:25]
	ds_write_b128 v174, v[2:5]
	ds_write_b128 v175, v[6:9]
	ds_write_b128 v176, v[10:13]
	ds_write_b128 v177, v[14:17] offset:128
	ds_write_b128 v178, v[18:21] offset:128
	ds_write_b128 v179, v[26:29] offset:128
	ds_write_b128 v180, v[30:33] offset:128
	ds_write_b128 v181, v[34:37] offset:256
	ds_write_b128 v182, v[38:41] offset:256
	ds_write_b128 v183, v[42:45] offset:256
	ds_write_b128 v184, v[46:49] offset:256
	ds_write_b128 v185, v[50:53] offset:384
	ds_write_b128 v186, v[54:57] offset:384
	ds_write_b128 v187, v[58:61] offset:384
	ds_write_b128 v188, v[62:65] offset:384
	s_cbranch_vccnz .Lp9_nonext
	s_ashr_i32 s48, s53, 2
	s_ashr_i32 s49, s48, 31
	s_lshl_b64 s[48:49], s[48:49], 17
	s_add_u32 s43, s29, s48
	s_addc_u32 s49, s30, s49
	s_and_b32 s48, s34, 0xc000
	s_add_u32 s48, s43, s48
	s_addc_u32 s49, s49, 0
	global_load_dwordx4 v[22:25], v66, s[48:49] nt
	global_load_dwordx4 v[2:5], v66, s[48:49] offset:1024 nt
	global_load_dwordx4 v[6:9], v66, s[48:49] offset:2048 nt
	s_nop 0
	global_load_dwordx4 v[10:13], v66, s[48:49] offset:3072 nt
	global_load_dwordx4 v[14:17], v74, s[48:49] nt
	s_nop 0
	global_load_dwordx4 v[18:21], v76, s[48:49] nt
	s_nop 0
	global_load_dwordx4 v[26:29], v78, s[48:49] nt
	s_nop 0
	global_load_dwordx4 v[30:33], v80, s[48:49] nt
	s_nop 0
	global_load_dwordx4 v[34:37], v82, s[48:49] nt
	s_nop 0
	global_load_dwordx4 v[38:41], v84, s[48:49] nt
	s_nop 0
	global_load_dwordx4 v[42:45], v86, s[48:49] nt
	s_nop 0
	global_load_dwordx4 v[46:49], v88, s[48:49] nt
	s_nop 0
	global_load_dwordx4 v[50:53], v90, s[48:49] nt
	s_nop 0
	global_load_dwordx4 v[54:57], v92, s[48:49] nt
	s_nop 0
	global_load_dwordx4 v[58:61], v94, s[48:49] nt
	s_nop 0
	global_load_dwordx4 v[62:65], v96, s[48:49] nt
	s_branch .LBB0_1466
